# recfin: hand-written fin epilogue (batched bias loads, scalar-advanced store base instead of 64-bit VALU address math per store) on top of v46
# speedup vs baseline: 1.0134x; 1.0134x over previous
.LBB6_72:
	s_or_b64 exec, exec, s[2:3]
	s_waitcnt vmcnt(18)
	v_lshrrev_b32_e32 v70, 6, v0
	v_lshrrev_b32_e32 v71, 5, v182
	s_waitcnt lgkmcnt(0)
	s_barrier
	ds_read_b128 v[66:69], v183 offset:4896
	ds_read_b128 v[86:89], v183
	s_waitcnt vmcnt(17) lgkmcnt(0)
	v_mfma_f32_32x32x16_f16 v[50:65], v[158:161], v[86:89], v[50:65]
	ds_read_b128 v[86:89], v183 offset:9792
	v_mfma_f32_32x32x16_f16 v[34:49], v[158:161], v[66:69], v[34:49]
	ds_read_b128 v[66:69], v183 offset:14688
	s_waitcnt lgkmcnt(1)
	v_mfma_f32_32x32x16_f16 v[18:33], v[158:161], v[86:89], v[18:33]
	ds_read_b128 v[86:89], v183 offset:64
	s_waitcnt lgkmcnt(1)
	v_mfma_f32_32x32x16_f16 v[2:17], v[158:161], v[66:69], v[2:17]
	ds_read_b128 v[66:69], v183 offset:4960
	s_waitcnt vmcnt(16) lgkmcnt(1)
	v_mfma_f32_32x32x16_f16 v[50:65], v[154:157], v[86:89], v[50:65]
	ds_read_b128 v[86:89], v183 offset:9856
	s_waitcnt lgkmcnt(1)
	v_mfma_f32_32x32x16_f16 v[34:49], v[154:157], v[66:69], v[34:49]
	ds_read_b128 v[66:69], v183 offset:14752
	s_waitcnt lgkmcnt(1)
	v_mfma_f32_32x32x16_f16 v[18:33], v[154:157], v[86:89], v[18:33]
	ds_read_b128 v[86:89], v183 offset:144
	s_waitcnt lgkmcnt(1)
	v_mfma_f32_32x32x16_f16 v[2:17], v[154:157], v[66:69], v[2:17]
	ds_read_b128 v[66:69], v183 offset:5040
	s_waitcnt vmcnt(15) lgkmcnt(1)
	v_mfma_f32_32x32x16_f16 v[50:65], v[146:149], v[86:89], v[50:65]
	ds_read_b128 v[86:89], v183 offset:9936
	s_waitcnt lgkmcnt(1)
	v_mfma_f32_32x32x16_f16 v[34:49], v[146:149], v[66:69], v[34:49]
	ds_read_b128 v[66:69], v183 offset:14832
	s_waitcnt lgkmcnt(1)
	v_mfma_f32_32x32x16_f16 v[18:33], v[146:149], v[86:89], v[18:33]
	ds_read_b128 v[86:89], v183 offset:208
	s_waitcnt lgkmcnt(1)
	v_mfma_f32_32x32x16_f16 v[2:17], v[146:149], v[66:69], v[2:17]
	ds_read_b128 v[66:69], v183 offset:5104
	s_waitcnt vmcnt(14) lgkmcnt(1)
	v_mfma_f32_32x32x16_f16 v[50:65], v[142:145], v[86:89], v[50:65]
	ds_read_b128 v[86:89], v183 offset:10000
	s_waitcnt lgkmcnt(1)
	v_mfma_f32_32x32x16_f16 v[34:49], v[142:145], v[66:69], v[34:49]
	ds_read_b128 v[66:69], v183 offset:14896
	s_waitcnt lgkmcnt(1)
	v_mfma_f32_32x32x16_f16 v[18:33], v[142:145], v[86:89], v[18:33]
	ds_read_b128 v[86:89], v183 offset:288
	s_waitcnt lgkmcnt(1)
	v_mfma_f32_32x32x16_f16 v[2:17], v[142:145], v[66:69], v[2:17]
	ds_read_b128 v[66:69], v183 offset:5184
	s_waitcnt vmcnt(13) lgkmcnt(1)
	v_mfma_f32_32x32x16_f16 v[50:65], v[134:137], v[86:89], v[50:65]
	ds_read_b128 v[86:89], v183 offset:10080
	s_waitcnt lgkmcnt(1)
	v_mfma_f32_32x32x16_f16 v[34:49], v[134:137], v[66:69], v[34:49]
	ds_read_b128 v[66:69], v183 offset:14976
	s_waitcnt lgkmcnt(1)
	v_mfma_f32_32x32x16_f16 v[18:33], v[134:137], v[86:89], v[18:33]
	ds_read_b128 v[86:89], v183 offset:352
	s_waitcnt lgkmcnt(1)
	v_mfma_f32_32x32x16_f16 v[2:17], v[134:137], v[66:69], v[2:17]
	ds_read_b128 v[66:69], v183 offset:5248
	s_waitcnt vmcnt(12) lgkmcnt(1)
	v_mfma_f32_32x32x16_f16 v[50:65], v[130:133], v[86:89], v[50:65]
	ds_read_b128 v[86:89], v183 offset:10144
	s_waitcnt lgkmcnt(1)
	v_mfma_f32_32x32x16_f16 v[34:49], v[130:133], v[66:69], v[34:49]
	ds_read_b128 v[66:69], v183 offset:15040
	s_waitcnt lgkmcnt(1)
	v_mfma_f32_32x32x16_f16 v[18:33], v[130:133], v[86:89], v[18:33]
	ds_read_b128 v[86:89], v183 offset:4896
	s_waitcnt lgkmcnt(1)
	v_mfma_f32_32x32x16_f16 v[2:17], v[130:133], v[66:69], v[2:17]
	ds_read_b128 v[66:69], v183 offset:9792
	s_waitcnt vmcnt(11) lgkmcnt(1)
	v_mfma_f32_32x32x16_f16 v[50:65], v[126:129], v[86:89], v[50:65]
	ds_read_b128 v[86:89], v183 offset:14688
	s_waitcnt lgkmcnt(1)
	v_mfma_f32_32x32x16_f16 v[34:49], v[126:129], v[66:69], v[34:49]
	ds_read_b128 v[66:69], v183 offset:19584
	s_waitcnt lgkmcnt(1)
	v_mfma_f32_32x32x16_f16 v[18:33], v[126:129], v[86:89], v[18:33]
	ds_read_b128 v[86:89], v183 offset:4960
	s_waitcnt lgkmcnt(1)
	v_mfma_f32_32x32x16_f16 v[2:17], v[126:129], v[66:69], v[2:17]
	ds_read_b128 v[66:69], v183 offset:9856
	s_waitcnt vmcnt(10) lgkmcnt(1)
	v_mfma_f32_32x32x16_f16 v[50:65], v[122:125], v[86:89], v[50:65]
	ds_read_b128 v[86:89], v183 offset:14752
	s_waitcnt lgkmcnt(1)
	v_mfma_f32_32x32x16_f16 v[34:49], v[122:125], v[66:69], v[34:49]
	ds_read_b128 v[66:69], v183 offset:19648
	s_waitcnt lgkmcnt(1)
	v_mfma_f32_32x32x16_f16 v[18:33], v[122:125], v[86:89], v[18:33]
	ds_read_b128 v[86:89], v183 offset:5040
	s_waitcnt lgkmcnt(1)
	v_mfma_f32_32x32x16_f16 v[2:17], v[122:125], v[66:69], v[2:17]
	ds_read_b128 v[66:69], v183 offset:9936
	s_waitcnt vmcnt(9) lgkmcnt(1)
	v_mfma_f32_32x32x16_f16 v[50:65], v[118:121], v[86:89], v[50:65]
	ds_read_b128 v[86:89], v183 offset:14832
	s_waitcnt lgkmcnt(1)
	v_mfma_f32_32x32x16_f16 v[34:49], v[118:121], v[66:69], v[34:49]
	ds_read_b128 v[66:69], v183 offset:19728
	s_waitcnt lgkmcnt(1)
	v_mfma_f32_32x32x16_f16 v[18:33], v[118:121], v[86:89], v[18:33]
	ds_read_b128 v[86:89], v183 offset:5104
	s_waitcnt lgkmcnt(1)
	v_mfma_f32_32x32x16_f16 v[2:17], v[118:121], v[66:69], v[2:17]
	ds_read_b128 v[66:69], v183 offset:10000
	s_waitcnt vmcnt(8) lgkmcnt(1)
	v_mfma_f32_32x32x16_f16 v[50:65], v[114:117], v[86:89], v[50:65]
	ds_read_b128 v[86:89], v183 offset:14896
	s_waitcnt lgkmcnt(1)
	v_mfma_f32_32x32x16_f16 v[34:49], v[114:117], v[66:69], v[34:49]
	ds_read_b128 v[66:69], v183 offset:19792
	s_waitcnt lgkmcnt(1)
	v_mfma_f32_32x32x16_f16 v[18:33], v[114:117], v[86:89], v[18:33]
	ds_read_b128 v[86:89], v183 offset:5184
	s_waitcnt lgkmcnt(1)
	v_mfma_f32_32x32x16_f16 v[2:17], v[114:117], v[66:69], v[2:17]
	ds_read_b128 v[66:69], v183 offset:10080
	s_waitcnt vmcnt(7) lgkmcnt(1)
	v_mfma_f32_32x32x16_f16 v[50:65], v[110:113], v[86:89], v[50:65]
	ds_read_b128 v[86:89], v183 offset:14976
	s_waitcnt lgkmcnt(1)
	v_mfma_f32_32x32x16_f16 v[34:49], v[110:113], v[66:69], v[34:49]
	ds_read_b128 v[66:69], v183 offset:19872
	s_waitcnt lgkmcnt(1)
	v_mfma_f32_32x32x16_f16 v[18:33], v[110:113], v[86:89], v[18:33]
	ds_read_b128 v[86:89], v183 offset:5248
	s_waitcnt lgkmcnt(1)
	v_mfma_f32_32x32x16_f16 v[2:17], v[110:113], v[66:69], v[2:17]
	ds_read_b128 v[66:69], v183 offset:10144
	s_waitcnt vmcnt(6) lgkmcnt(1)
	v_mfma_f32_32x32x16_f16 v[50:65], v[106:109], v[86:89], v[50:65]
	ds_read_b128 v[86:89], v183 offset:15040
	s_waitcnt lgkmcnt(1)
	v_mfma_f32_32x32x16_f16 v[34:49], v[106:109], v[66:69], v[34:49]
	ds_read_b128 v[66:69], v183 offset:19936
	s_waitcnt lgkmcnt(1)
	v_mfma_f32_32x32x16_f16 v[18:33], v[106:109], v[86:89], v[18:33]
	ds_read_b128 v[86:89], v183 offset:9792
	s_waitcnt lgkmcnt(1)
	v_mfma_f32_32x32x16_f16 v[2:17], v[106:109], v[66:69], v[2:17]
	ds_read_b128 v[66:69], v183 offset:14688
	s_waitcnt vmcnt(5) lgkmcnt(1)
	v_mfma_f32_32x32x16_f16 v[50:65], v[102:105], v[86:89], v[50:65]
	ds_read_b128 v[86:89], v183 offset:19584
	s_waitcnt lgkmcnt(1)
	v_mfma_f32_32x32x16_f16 v[34:49], v[102:105], v[66:69], v[34:49]
	ds_read_b128 v[66:69], v183 offset:24480
	s_waitcnt lgkmcnt(1)
	v_mfma_f32_32x32x16_f16 v[18:33], v[102:105], v[86:89], v[18:33]
	ds_read_b128 v[86:89], v183 offset:9856
	s_waitcnt lgkmcnt(1)
	v_mfma_f32_32x32x16_f16 v[2:17], v[102:105], v[66:69], v[2:17]
	ds_read_b128 v[66:69], v183 offset:14752
	s_waitcnt vmcnt(4) lgkmcnt(1)
	v_mfma_f32_32x32x16_f16 v[50:65], v[94:97], v[86:89], v[50:65]
	ds_read_b128 v[86:89], v183 offset:19648
	s_waitcnt lgkmcnt(1)
	v_mfma_f32_32x32x16_f16 v[34:49], v[94:97], v[66:69], v[34:49]
	ds_read_b128 v[66:69], v183 offset:24544
	s_waitcnt lgkmcnt(1)
	v_mfma_f32_32x32x16_f16 v[18:33], v[94:97], v[86:89], v[18:33]
	ds_read_b128 v[86:89], v183 offset:9936
	s_waitcnt lgkmcnt(1)
	v_mfma_f32_32x32x16_f16 v[2:17], v[94:97], v[66:69], v[2:17]
	ds_read_b128 v[66:69], v183 offset:14832
	s_waitcnt vmcnt(3) lgkmcnt(1)
	v_mfma_f32_32x32x16_f16 v[50:65], v[90:93], v[86:89], v[50:65]
	ds_read_b128 v[86:89], v183 offset:19728
	s_waitcnt lgkmcnt(1)
	v_mfma_f32_32x32x16_f16 v[34:49], v[90:93], v[66:69], v[34:49]
	ds_read_b128 v[66:69], v183 offset:24624
	s_waitcnt lgkmcnt(1)
	v_mfma_f32_32x32x16_f16 v[18:33], v[90:93], v[86:89], v[18:33]
	ds_read_b128 v[86:89], v183 offset:10000
	s_waitcnt lgkmcnt(1)
	v_mfma_f32_32x32x16_f16 v[2:17], v[90:93], v[66:69], v[2:17]
	ds_read_b128 v[66:69], v183 offset:14896
	s_waitcnt vmcnt(2) lgkmcnt(1)
	v_mfma_f32_32x32x16_f16 v[50:65], v[82:85], v[86:89], v[50:65]
	ds_read_b128 v[86:89], v183 offset:19792
	s_waitcnt lgkmcnt(1)
	v_mfma_f32_32x32x16_f16 v[34:49], v[82:85], v[66:69], v[34:49]
	ds_read_b128 v[66:69], v183 offset:24688
	s_waitcnt lgkmcnt(1)
	v_mfma_f32_32x32x16_f16 v[18:33], v[82:85], v[86:89], v[18:33]
	ds_read_b128 v[86:89], v183 offset:10080
	s_waitcnt lgkmcnt(1)
	v_mfma_f32_32x32x16_f16 v[2:17], v[82:85], v[66:69], v[2:17]
	ds_read_b128 v[66:69], v183 offset:14976
	s_waitcnt vmcnt(1) lgkmcnt(1)
	v_mfma_f32_32x32x16_f16 v[50:65], v[78:81], v[86:89], v[50:65]
	ds_read_b128 v[82:85], v183 offset:19872
	s_waitcnt lgkmcnt(1)
	v_mfma_f32_32x32x16_f16 v[34:49], v[78:81], v[66:69], v[34:49]
	ds_read_b128 v[66:69], v183 offset:24768
	s_waitcnt lgkmcnt(1)
	v_mfma_f32_32x32x16_f16 v[18:33], v[78:81], v[82:85], v[18:33]
	ds_read_b128 v[82:85], v183 offset:10144
	s_waitcnt lgkmcnt(1)
	v_mfma_f32_32x32x16_f16 v[2:17], v[78:81], v[66:69], v[2:17]
	ds_read_b128 v[66:69], v183 offset:15040
	s_waitcnt vmcnt(0) lgkmcnt(1)
	v_mfma_f32_32x32x16_f16 v[50:65], v[74:77], v[82:85], v[50:65]
	ds_read_b128 v[78:81], v183 offset:19936
	s_waitcnt lgkmcnt(1)
	v_mfma_f32_32x32x16_f16 v[34:49], v[74:77], v[66:69], v[34:49]
	ds_read_b128 v[66:69], v183 offset:24832
	s_waitcnt lgkmcnt(1)
	v_mfma_f32_32x32x16_f16 v[18:33], v[74:77], v[78:81], v[18:33]
	s_waitcnt lgkmcnt(0)
	v_mfma_f32_32x32x16_f16 v[2:17], v[74:77], v[66:69], v[2:17]
	v_lshlrev_b32_e32 v66, 2, v71
	v_lshl_or_b32 v74, v70, 5, v66
	v_lshlrev_b32_e32 v80, 2, v74
	s_barrier
	global_load_dwordx4 v[76:79], v80, s[16:17]
	v_lshlrev_b32_e32 v66, 7, v70
	s_movk_i32 s3, 0x210
	v_lshl_or_b32 v66, v71, 3, v66
	v_mad_u32_u24 v73, v180, s3, v66
	global_load_dwordx4 v[66:69], v80, s[16:17] offset:32
	s_mov_b32 s2, 0x41800000
	v_add_u32_e32 v72, 0x4000, v73
	v_add_u32_e32 v71, 0x8000, v73
	s_waitcnt vmcnt(1)
	v_fmamk_f32 v50, v50, 0x3a800000, v76
	v_fmamk_f32 v51, v51, 0x3a800000, v77
	v_fmamk_f32 v52, v52, 0x3a800000, v78
	v_fmamk_f32 v53, v53, 0x3a800000, v79
	v_fmamk_f32 v34, v34, 0x3a800000, v76
	v_fmamk_f32 v35, v35, 0x3a800000, v77
	v_fmamk_f32 v36, v36, 0x3a800000, v78
	v_fmamk_f32 v37, v37, 0x3a800000, v79
	v_fmamk_f32 v18, v18, 0x3a800000, v76
	v_fmamk_f32 v19, v19, 0x3a800000, v77
	v_fmamk_f32 v20, v20, 0x3a800000, v78
	v_fmamk_f32 v21, v21, 0x3a800000, v79
	v_fmamk_f32 v75, v2, 0x3a800000, v76
	v_fmamk_f32 v76, v3, 0x3a800000, v77
	v_fmamk_f32 v77, v4, 0x3a800000, v78
	v_fmac_f32_e32 v79, 0x3a800000, v5
	v_max_f32_e32 v78, 0, v50
	v_max_f32_e32 v81, 0, v51
	v_max_f32_e32 v2, 0, v52
	v_max_f32_e32 v3, 0, v53
	v_max_f32_e32 v82, 0, v34
	v_max_f32_e32 v88, 0, v35
	v_max_f32_e32 v4, 0, v36
	v_max_f32_e32 v5, 0, v37
	v_max_f32_e32 v84, 0, v18
	v_max_f32_e32 v92, 0, v19
	v_max_f32_e32 v18, 0, v20
	v_max_f32_e32 v19, 0, v21
	v_max_f32_e32 v93, 0, v76
	v_max_f32_e32 v20, 0, v77
	v_max_f32_e32 v21, 0, v79
	v_mul_f32_e32 v77, 0x41800000, v78
	v_fma_mixlo_f16 v76, v78, s2, 0
	v_mul_f32_e32 v79, 0x41800000, v81
	v_pk_mul_f32 v[34:35], v[2:3], s[2:3] op_sel_hi:[1,0]
	v_fma_mixlo_f16 v86, v81, s2, 0
	v_mul_f32_e32 v83, 0x41800000, v82
	v_fma_mixlo_f16 v85, v82, s2, 0
	v_mul_f32_e32 v87, 0x41800000, v88
	v_pk_mul_f32 v[36:37], v[4:5], s[2:3] op_sel_hi:[1,0]
	v_fma_mixlo_f16 v76, v78, s2, -v76 op_sel_hi:[0,0,1]
	v_cvt_pk_f16_f32 v78, v77, v79
	v_cvt_pk_f16_f32 v79, v34, v35
	v_fma_mixlo_f16 v89, v88, s2, 0
	v_fma_mixlo_f16 v34, v82, s2, -v85 op_sel_hi:[0,0,1]
	v_cvt_pk_f16_f32 v82, v83, v87
	v_cvt_pk_f16_f32 v83, v36, v37
	v_fma_mixhi_f16 v76, v81, s2, -v86 op_sel_hi:[0,0,1]
	v_cvt_f32_f16_e32 v86, v79
	v_cvt_f32_f16_sdwa v87, v79 dst_sel:DWORD dst_unused:UNUSED_PAD src0_sel:WORD_1
	v_fma_mixhi_f16 v34, v88, s2, -v89 op_sel_hi:[0,0,1]
	v_cvt_f32_f16_e32 v88, v83
	v_cvt_f32_f16_sdwa v89, v83 dst_sel:DWORD dst_unused:UNUSED_PAD src0_sel:WORD_1
	v_pk_mul_f32 v[50:51], v[18:19], s[2:3] op_sel_hi:[1,0]
	v_mul_f32_e32 v90, 0x41800000, v84
	v_fma_mixlo_f16 v91, v84, s2, 0
	v_mul_f32_e32 v94, 0x41800000, v92
	v_pk_mul_f32 v[52:53], v[20:21], s[2:3] op_sel_hi:[1,0]
	v_cvt_pk_f16_f32 v85, v50, v51
	v_pk_fma_f32 v[2:3], v[2:3], s[2:3], v[86:87] op_sel_hi:[1,0,1] neg_lo:[0,0,1] neg_hi:[0,0,1]
	v_fma_mixlo_f16 v36, v84, s2, -v91 op_sel_hi:[0,0,1]
	v_cvt_pk_f16_f32 v84, v90, v94
	v_cvt_f32_f16_e32 v90, v85
	v_cvt_f32_f16_sdwa v91, v85 dst_sel:DWORD dst_unused:UNUSED_PAD src0_sel:WORD_1
	v_pk_fma_f32 v[4:5], v[4:5], s[2:3], v[88:89] op_sel_hi:[1,0,1] neg_lo:[0,0,1] neg_hi:[0,0,1]
	v_cvt_pk_f16_f32 v77, v2, v3
	v_cvt_pk_f16_f32 v3, v52, v53
	v_cvt_pk_f16_f32 v35, v4, v5
	v_cvt_f32_f16_e32 v4, v3
	v_cvt_f32_f16_sdwa v5, v3 dst_sel:DWORD dst_unused:UNUSED_PAD src0_sel:WORD_1
	v_max_f32_e32 v75, 0, v75
	v_fma_mixlo_f16 v97, v75, s2, 0
	v_pk_fma_f32 v[18:19], v[18:19], s[2:3], v[90:91] op_sel_hi:[1,0,1] neg_lo:[0,0,1] neg_hi:[0,0,1]
	v_mul_f32_e32 v96, 0x41800000, v75
	v_mul_f32_e32 v98, 0x41800000, v93
	v_fma_mixlo_f16 v50, v75, s2, -v97 op_sel_hi:[0,0,1]
	v_cvt_pk_f16_f32 v37, v18, v19
	v_fma_mixlo_f16 v18, v93, s2, 0
	v_pk_fma_f32 v[4:5], v[20:21], s[2:3], v[4:5] op_sel_hi:[1,0,1] neg_lo:[0,0,1] neg_hi:[0,0,1]
	v_fma_mixlo_f16 v95, v92, s2, 0
	v_cvt_pk_f16_f32 v2, v96, v98
	v_fma_mixhi_f16 v50, v93, s2, -v18 op_sel_hi:[0,0,1]
	v_cvt_pk_f16_f32 v51, v4, v5
	v_add_u32_e32 v18, 0xc000, v73
	v_fma_mixhi_f16 v36, v92, s2, -v95 op_sel_hi:[0,0,1]
	ds_write2_b64 v73, v[78:79], v[76:77] offset1:2
	ds_write2_b64 v72, v[82:83], v[34:35] offset0:64 offset1:66
	ds_write2_b64 v71, v[84:85], v[36:37] offset0:128 offset1:130
	ds_write2_b64 v18, v[2:3], v[50:51] offset0:192 offset1:194
	s_waitcnt vmcnt(0)
	v_fmamk_f32 v2, v54, 0x3a800000, v66
	v_max_f32_e32 v2, 0, v2
	v_fma_mixlo_f16 v3, v2, s2, 0
	v_mul_f32_e32 v19, 0x41800000, v2
	v_fma_mixlo_f16 v20, v2, s2, -v3 op_sel_hi:[0,0,1]
	v_fmamk_f32 v2, v55, 0x3a800000, v67
	v_max_f32_e32 v21, 0, v2
	v_fmamk_f32 v2, v56, 0x3a800000, v68
	v_fmamk_f32 v35, v57, 0x3a800000, v69
	v_max_f32_e32 v34, 0, v2
	v_max_f32_e32 v35, 0, v35
	v_pk_mul_f32 v[36:37], v[34:35], s[2:3] op_sel_hi:[1,0]
	global_load_dwordx4 v[2:5], v80, s[16:17] offset:64
	v_cvt_pk_f16_f32 v37, v36, v37
	v_cvt_f32_f16_e32 v50, v37
	v_cvt_f32_f16_sdwa v51, v37 dst_sel:DWORD dst_unused:UNUSED_PAD src0_sel:WORD_1
	v_fma_mixlo_f16 v53, v21, s2, 0
	v_mul_f32_e32 v52, 0x41800000, v21
	v_fma_mixhi_f16 v20, v21, s2, -v53 op_sel_hi:[0,0,1]
	v_pk_fma_f32 v[34:35], v[34:35], s[2:3], v[50:51] op_sel_hi:[1,0,1] neg_lo:[0,0,1] neg_hi:[0,0,1]
	v_cvt_pk_f16_f32 v36, v19, v52
	v_cvt_pk_f16_f32 v21, v34, v35
	v_fmamk_f32 v34, v40, 0x3a800000, v68
	v_fmamk_f32 v35, v41, 0x3a800000, v69
	v_fmamk_f32 v19, v38, 0x3a800000, v66
	v_max_f32_e32 v34, 0, v34
	v_max_f32_e32 v35, 0, v35
	ds_write2_b64 v73, v[36:37], v[20:21] offset0:4 offset1:6
	v_max_f32_e32 v19, 0, v19
	v_pk_mul_f32 v[36:37], v[34:35], s[2:3] op_sel_hi:[1,0]
	v_fma_mixlo_f16 v20, v19, s2, 0
	v_cvt_pk_f16_f32 v37, v36, v37
	v_mul_f32_e32 v21, 0x41800000, v19
	v_fma_mixlo_f16 v20, v19, s2, -v20 op_sel_hi:[0,0,1]
	v_fmamk_f32 v19, v39, 0x3a800000, v67
	v_cvt_f32_f16_e32 v38, v37
	v_cvt_f32_f16_sdwa v39, v37 dst_sel:DWORD dst_unused:UNUSED_PAD src0_sel:WORD_1
	v_max_f32_e32 v19, 0, v19
	v_fma_mixlo_f16 v40, v19, s2, 0
	v_mul_f32_e32 v50, 0x41800000, v19
	v_fma_mixhi_f16 v20, v19, s2, -v40 op_sel_hi:[0,0,1]
	v_pk_fma_f32 v[34:35], v[34:35], s[2:3], v[38:39] op_sel_hi:[1,0,1] neg_lo:[0,0,1] neg_hi:[0,0,1]
	v_fmamk_f32 v19, v22, 0x3a800000, v66
	v_cvt_pk_f16_f32 v36, v21, v50
	v_cvt_pk_f16_f32 v21, v34, v35
	v_max_f32_e32 v19, 0, v19
	ds_write2_b64 v72, v[36:37], v[20:21] offset0:68 offset1:70
	v_fma_mixlo_f16 v20, v19, s2, 0
	v_mul_f32_e32 v21, 0x41800000, v19
	v_fma_mixlo_f16 v20, v19, s2, -v20 op_sel_hi:[0,0,1]
	v_fmamk_f32 v19, v23, 0x3a800000, v67
	v_fmamk_f32 v22, v24, 0x3a800000, v68
	v_fmamk_f32 v23, v25, 0x3a800000, v69
	v_max_f32_e32 v22, 0, v22
	v_max_f32_e32 v23, 0, v23
	v_pk_mul_f32 v[24:25], v[22:23], s[2:3] op_sel_hi:[1,0]
	v_max_f32_e32 v19, 0, v19
	v_cvt_pk_f16_f32 v25, v24, v25
	v_cvt_f32_f16_e32 v34, v25
	v_cvt_f32_f16_sdwa v35, v25 dst_sel:DWORD dst_unused:UNUSED_PAD src0_sel:WORD_1
	v_mul_f32_e32 v36, 0x41800000, v19
	v_fma_mixlo_f16 v37, v19, s2, 0
	v_fmamk_f32 v6, v6, 0x3a800000, v66
	v_pk_fma_f32 v[22:23], v[22:23], s[2:3], v[34:35] op_sel_hi:[1,0,1] neg_lo:[0,0,1] neg_hi:[0,0,1]
	v_cvt_pk_f16_f32 v24, v21, v36
	v_fma_mixhi_f16 v20, v19, s2, -v37 op_sel_hi:[0,0,1]
	v_cvt_pk_f16_f32 v21, v22, v23
	v_max_f32_e32 v6, 0, v6
	v_fmamk_f32 v8, v8, 0x3a800000, v68
	v_fmac_f32_e32 v69, 0x3a800000, v9
	ds_write2_b64 v71, v[24:25], v[20:21] offset0:132 offset1:134
	v_fma_mixlo_f16 v20, v6, s2, 0
	v_max_f32_e32 v8, 0, v8
	v_max_f32_e32 v9, 0, v69
	v_mul_f32_e32 v19, 0x41800000, v6
	v_fma_mixlo_f16 v6, v6, s2, -v20 op_sel_hi:[0,0,1]
	v_pk_mul_f32 v[20:21], v[8:9], s[2:3] op_sel_hi:[1,0]
	v_fmamk_f32 v7, v7, 0x3a800000, v67
	v_cvt_pk_f16_f32 v21, v20, v21
	v_cvt_f32_f16_e32 v22, v21
	v_cvt_f32_f16_sdwa v23, v21 dst_sel:DWORD dst_unused:UNUSED_PAD src0_sel:WORD_1
	v_max_f32_e32 v7, 0, v7
	v_mul_f32_e32 v24, 0x41800000, v7
	v_fma_mixlo_f16 v25, v7, s2, 0
	v_pk_fma_f32 v[8:9], v[8:9], s[2:3], v[22:23] op_sel_hi:[1,0,1] neg_lo:[0,0,1] neg_hi:[0,0,1]
	v_cvt_pk_f16_f32 v20, v19, v24
	v_fma_mixhi_f16 v6, v7, s2, -v25 op_sel_hi:[0,0,1]
	v_cvt_pk_f16_f32 v7, v8, v9
	ds_write2_b64 v18, v[20:21], v[6:7] offset0:196 offset1:198
	global_load_dwordx4 v[6:9], v80, s[16:17] offset:96
	s_waitcnt vmcnt(1)
	v_fmamk_f32 v22, v60, 0x3a800000, v4
	v_fmamk_f32 v23, v61, 0x3a800000, v5
	v_max_f32_e32 v22, 0, v22
	v_max_f32_e32 v23, 0, v23
	v_pk_mul_f32 v[24:25], v[22:23], s[2:3] op_sel_hi:[1,0]
	v_fmamk_f32 v19, v58, 0x3a800000, v2
	v_cvt_pk_f16_f32 v25, v24, v25
	v_max_f32_e32 v19, 0, v19
	v_cvt_f32_f16_e32 v34, v25
	v_cvt_f32_f16_sdwa v35, v25 dst_sel:DWORD dst_unused:UNUSED_PAD src0_sel:WORD_1
	v_fma_mixlo_f16 v20, v19, s2, 0
	v_mul_f32_e32 v21, 0x41800000, v19
	v_fma_mixlo_f16 v20, v19, s2, -v20 op_sel_hi:[0,0,1]
	v_fmamk_f32 v19, v59, 0x3a800000, v3
	v_max_f32_e32 v19, 0, v19
	v_mul_f32_e32 v36, 0x41800000, v19
	v_pk_fma_f32 v[22:23], v[22:23], s[2:3], v[34:35] op_sel_hi:[1,0,1] neg_lo:[0,0,1] neg_hi:[0,0,1]
	v_fma_mixlo_f16 v37, v19, s2, 0
	v_cvt_pk_f16_f32 v24, v21, v36
	v_cvt_pk_f16_f32 v21, v22, v23
	v_fmamk_f32 v22, v44, 0x3a800000, v4
	v_fmamk_f32 v23, v45, 0x3a800000, v5
	v_fma_mixhi_f16 v20, v19, s2, -v37 op_sel_hi:[0,0,1]
	v_max_f32_e32 v22, 0, v22
	v_max_f32_e32 v23, 0, v23
	ds_write2_b64 v73, v[24:25], v[20:21] offset0:8 offset1:10
	v_fmamk_f32 v19, v42, 0x3a800000, v2
	v_pk_mul_f32 v[24:25], v[22:23], s[2:3] op_sel_hi:[1,0]
	v_max_f32_e32 v19, 0, v19
	v_cvt_pk_f16_f32 v25, v24, v25
	v_fma_mixlo_f16 v20, v19, s2, 0
	v_cvt_f32_f16_e32 v34, v25
	v_cvt_f32_f16_sdwa v35, v25 dst_sel:DWORD dst_unused:UNUSED_PAD src0_sel:WORD_1
	v_mul_f32_e32 v21, 0x41800000, v19
	v_fma_mixlo_f16 v20, v19, s2, -v20 op_sel_hi:[0,0,1]
	v_fmamk_f32 v19, v43, 0x3a800000, v3
	v_max_f32_e32 v19, 0, v19
	v_fma_mixlo_f16 v37, v19, s2, 0
	v_mul_f32_e32 v36, 0x41800000, v19
	v_fma_mixhi_f16 v20, v19, s2, -v37 op_sel_hi:[0,0,1]
	v_pk_fma_f32 v[22:23], v[22:23], s[2:3], v[34:35] op_sel_hi:[1,0,1] neg_lo:[0,0,1] neg_hi:[0,0,1]
	v_fmamk_f32 v19, v26, 0x3a800000, v2
	v_cvt_pk_f16_f32 v24, v21, v36
	v_cvt_pk_f16_f32 v21, v22, v23
	v_max_f32_e32 v19, 0, v19
	ds_write2_b64 v72, v[24:25], v[20:21] offset0:72 offset1:74
	v_fma_mixlo_f16 v20, v19, s2, 0
	v_fmamk_f32 v22, v28, 0x3a800000, v4
	v_fmamk_f32 v23, v29, 0x3a800000, v5
	v_mul_f32_e32 v21, 0x41800000, v19
	v_fma_mixlo_f16 v20, v19, s2, -v20 op_sel_hi:[0,0,1]
	v_fmamk_f32 v19, v27, 0x3a800000, v3
	v_max_f32_e32 v22, 0, v22
	v_max_f32_e32 v23, 0, v23
	v_fmamk_f32 v2, v10, 0x3a800000, v2
	v_max_f32_e32 v19, 0, v19
	v_pk_mul_f32 v[24:25], v[22:23], s[2:3] op_sel_hi:[1,0]
	v_max_f32_e32 v2, 0, v2
	v_fmamk_f32 v4, v12, 0x3a800000, v4
	v_fmac_f32_e32 v5, 0x3a800000, v13
	v_cvt_pk_f16_f32 v25, v24, v25
	v_fma_mixlo_f16 v28, v19, s2, 0
	v_fma_mixlo_f16 v10, v2, s2, 0
	v_max_f32_e32 v4, 0, v4
	v_max_f32_e32 v5, 0, v5
	v_mul_f32_e32 v34, 0x41800000, v19
	v_cvt_f32_f16_e32 v26, v25
	v_cvt_f32_f16_sdwa v27, v25 dst_sel:DWORD dst_unused:UNUSED_PAD src0_sel:WORD_1
	v_fma_mixhi_f16 v20, v19, s2, -v28 op_sel_hi:[0,0,1]
	v_mul_f32_e32 v19, 0x41800000, v2
	v_fma_mixlo_f16 v2, v2, s2, -v10 op_sel_hi:[0,0,1]
	v_fmamk_f32 v3, v11, 0x3a800000, v3
	v_pk_mul_f32 v[10:11], v[4:5], s[2:3] op_sel_hi:[1,0]
	v_pk_fma_f32 v[22:23], v[22:23], s[2:3], v[26:27] op_sel_hi:[1,0,1] neg_lo:[0,0,1] neg_hi:[0,0,1]
	v_cvt_pk_f16_f32 v11, v10, v11
	v_cvt_f32_f16_e32 v12, v11
	v_cvt_f32_f16_sdwa v13, v11 dst_sel:DWORD dst_unused:UNUSED_PAD src0_sel:WORD_1
	v_cvt_pk_f16_f32 v24, v21, v34
	v_cvt_pk_f16_f32 v21, v22, v23
	v_max_f32_e32 v3, 0, v3
	ds_write2_b64 v71, v[24:25], v[20:21] offset0:136 offset1:138
	v_mul_f32_e32 v20, 0x41800000, v3
	v_fma_mixlo_f16 v21, v3, s2, 0
	v_pk_fma_f32 v[4:5], v[4:5], s[2:3], v[12:13] op_sel_hi:[1,0,1] neg_lo:[0,0,1] neg_hi:[0,0,1]
	v_cvt_pk_f16_f32 v10, v19, v20
	v_fma_mixhi_f16 v2, v3, s2, -v21 op_sel_hi:[0,0,1]
	v_cvt_pk_f16_f32 v3, v4, v5
	ds_write2_b64 v18, v[10:11], v[2:3] offset0:200 offset1:202
	s_waitcnt vmcnt(0)
	v_fmamk_f32 v2, v62, 0x3a800000, v6
	v_max_f32_e32 v2, 0, v2
	v_fma_mixlo_f16 v4, v2, s2, 0
	v_mul_f32_e32 v3, 0x41800000, v2
	v_fma_mixlo_f16 v2, v2, s2, -v4 op_sel_hi:[0,0,1]
	v_fmamk_f32 v4, v63, 0x3a800000, v7
	v_max_f32_e32 v19, 0, v4
	v_fmamk_f32 v4, v64, 0x3a800000, v8
	v_fmamk_f32 v5, v65, 0x3a800000, v9
	v_max_f32_e32 v4, 0, v4
	v_max_f32_e32 v5, 0, v5
	v_pk_mul_f32 v[10:11], v[4:5], s[2:3] op_sel_hi:[1,0]
	v_mul_f32_e32 v20, 0x41800000, v19
	v_cvt_pk_f16_f32 v11, v10, v11
	v_cvt_f32_f16_e32 v12, v11
	v_cvt_f32_f16_sdwa v13, v11 dst_sel:DWORD dst_unused:UNUSED_PAD src0_sel:WORD_1
	v_fma_mixlo_f16 v21, v19, s2, 0
	v_cvt_pk_f16_f32 v10, v3, v20
	v_fma_mixhi_f16 v2, v19, s2, -v21 op_sel_hi:[0,0,1]
	v_pk_fma_f32 v[4:5], v[4:5], s[2:3], v[12:13] op_sel_hi:[1,0,1] neg_lo:[0,0,1] neg_hi:[0,0,1]
	s_nop 0
	v_cvt_pk_f16_f32 v3, v4, v5
	ds_write2_b64 v73, v[10:11], v[2:3] offset0:12 offset1:14
	v_fmamk_f32 v2, v46, 0x3a800000, v6
	v_max_f32_e32 v2, 0, v2
	v_fma_mixlo_f16 v4, v2, s2, 0
	v_mul_f32_e32 v3, 0x41800000, v2
	v_fma_mixlo_f16 v2, v2, s2, -v4 op_sel_hi:[0,0,1]
	v_fmamk_f32 v4, v47, 0x3a800000, v7
	v_max_f32_e32 v19, 0, v4
	v_fmamk_f32 v4, v48, 0x3a800000, v8
	v_fmamk_f32 v5, v49, 0x3a800000, v9
	v_max_f32_e32 v4, 0, v4
	v_max_f32_e32 v5, 0, v5
	v_pk_mul_f32 v[10:11], v[4:5], s[2:3] op_sel_hi:[1,0]
	v_mul_f32_e32 v20, 0x41800000, v19
	v_cvt_pk_f16_f32 v11, v10, v11
	v_cvt_f32_f16_e32 v12, v11
	v_cvt_f32_f16_sdwa v13, v11 dst_sel:DWORD dst_unused:UNUSED_PAD src0_sel:WORD_1
	v_fma_mixlo_f16 v21, v19, s2, 0
	v_cvt_pk_f16_f32 v10, v3, v20
	v_fma_mixhi_f16 v2, v19, s2, -v21 op_sel_hi:[0,0,1]
	v_pk_fma_f32 v[4:5], v[4:5], s[2:3], v[12:13] op_sel_hi:[1,0,1] neg_lo:[0,0,1] neg_hi:[0,0,1]
	s_nop 0
	v_cvt_pk_f16_f32 v3, v4, v5
	ds_write2_b64 v72, v[10:11], v[2:3] offset0:76 offset1:78
	v_fmamk_f32 v2, v30, 0x3a800000, v6
	v_max_f32_e32 v2, 0, v2
	v_fma_mixlo_f16 v4, v2, s2, 0
	v_mul_f32_e32 v3, 0x41800000, v2
	v_fma_mixlo_f16 v2, v2, s2, -v4 op_sel_hi:[0,0,1]
	v_fmamk_f32 v4, v31, 0x3a800000, v7
	v_max_f32_e32 v19, 0, v4
	v_fmamk_f32 v4, v32, 0x3a800000, v8
	v_fmamk_f32 v5, v33, 0x3a800000, v9
	v_max_f32_e32 v4, 0, v4
	v_max_f32_e32 v5, 0, v5
	v_pk_mul_f32 v[10:11], v[4:5], s[2:3] op_sel_hi:[1,0]
	v_mul_f32_e32 v20, 0x41800000, v19
	v_cvt_pk_f16_f32 v11, v10, v11
	v_cvt_f32_f16_e32 v12, v11
	v_cvt_f32_f16_sdwa v13, v11 dst_sel:DWORD dst_unused:UNUSED_PAD src0_sel:WORD_1
	v_fma_mixlo_f16 v21, v19, s2, 0
	v_cvt_pk_f16_f32 v10, v3, v20
	v_fma_mixhi_f16 v2, v19, s2, -v21 op_sel_hi:[0,0,1]
	v_pk_fma_f32 v[4:5], v[4:5], s[2:3], v[12:13] op_sel_hi:[1,0,1] neg_lo:[0,0,1] neg_hi:[0,0,1]
	v_fmac_f32_e32 v9, 0x3a800000, v17
	v_cvt_pk_f16_f32 v3, v4, v5
	ds_write2_b64 v71, v[10:11], v[2:3] offset0:140 offset1:142
	v_fmamk_f32 v2, v14, 0x3a800000, v6
	v_max_f32_e32 v2, 0, v2
	v_fma_mixlo_f16 v4, v2, s2, 0
	v_mul_f32_e32 v3, 0x41800000, v2
	v_fma_mixlo_f16 v2, v2, s2, -v4 op_sel_hi:[0,0,1]
	v_fmamk_f32 v4, v15, 0x3a800000, v7
	v_max_f32_e32 v10, 0, v4
	v_fmamk_f32 v4, v16, 0x3a800000, v8
	v_max_f32_e32 v4, 0, v4
	v_max_f32_e32 v5, 0, v9
	v_pk_mul_f32 v[6:7], v[4:5], s[2:3] op_sel_hi:[1,0]
	v_fma_mixlo_f16 v12, v10, s2, 0
	v_cvt_pk_f16_f32 v7, v6, v7
	v_cvt_f32_f16_e32 v8, v7
	v_cvt_f32_f16_sdwa v9, v7 dst_sel:DWORD dst_unused:UNUSED_PAD src0_sel:WORD_1
	v_mul_f32_e32 v11, 0x41800000, v10
	v_fma_mixhi_f16 v2, v10, s2, -v12 op_sel_hi:[0,0,1]
	v_cvt_pk_f16_f32 v6, v3, v11
	v_pk_fma_f32 v[4:5], v[4:5], s[2:3], v[8:9] op_sel_hi:[1,0,1] neg_lo:[0,0,1] neg_hi:[0,0,1]
	s_movk_i32 s2, 0x80
	v_cvt_pk_f16_f32 v3, v4, v5
	v_cmp_gt_u32_e32 vcc, s2, v0
	ds_write2_b64 v18, v[6:7], v[2:3] offset0:204 offset1:206
	s_waitcnt lgkmcnt(0)
	s_barrier
	s_and_saveexec_b64 s[2:3], vcc
	s_cbranch_execz .LBB6_74
	v_mov_b32_e32 v3, 0
	v_lshlrev_b32_e32 v2, 4, v1
	v_lshl_add_u64 v[0:1], s[0:1], 0, v[2:3]
	v_lshlrev_b32_e32 v2, 11, v70
	v_lshl_add_u64 v[72:73], v[0:1], 0, v[2:3]
	v_add_co_u32_e32 v4, vcc, 0x1000, v72
	s_nop 1
	v_addc_co_u32_e32 v5, vcc, 0, v73, vcc
	global_load_dwordx4 v[0:3], v[72:73], off
	global_load_dwordx4 v[64:67], v[4:5], off
	v_mul_u32_u24_e32 v4, 0x210, v180
	v_add_u32_e32 v75, v4, v181
	ds_read_b128 v[4:7], v75
	ds_read_b128 v[68:71], v75 offset:64
	ds_read_b128 v[8:11], v75 offset:16896
	ds_read_b128 v[76:79], v75 offset:16960
	ds_read_b128 v[12:15], v75 offset:33792
	ds_read_b128 v[82:85], v75 offset:33856
	ds_read_b128 v[86:89], v75 offset:50688
	ds_read_b128 v[90:93], v75 offset:50752
	s_waitcnt vmcnt(1) lgkmcnt(7)
	v_mfma_f32_32x32x16_f16 v[48:63], v[0:3], v[4:7], 0
	s_waitcnt lgkmcnt(5)
	v_mfma_f32_32x32x16_f16 v[32:47], v[0:3], v[8:11], 0
	s_waitcnt lgkmcnt(3)
	v_mfma_f32_32x32x16_f16 v[16:31], v[0:3], v[12:15], 0
	s_waitcnt lgkmcnt(1)
	v_mfma_f32_32x32x16_f16 v[0:15], v[0:3], v[86:89], 0
	s_movk_i32 s0, 0x3000
	v_add_co_u32_e32 v110, vcc, s0, v72
	s_nop 1
	v_addc_co_u32_e32 v111, vcc, 0, v73, vcc
	global_load_dwordx4 v[86:89], v[110:111], off offset:-4096
	ds_read_b128 v[94:97], v75 offset:128
	ds_read_b128 v[98:101], v75 offset:17024
	ds_read_b128 v[102:105], v75 offset:33920
	ds_read_b128 v[106:109], v75 offset:50816
	s_waitcnt vmcnt(1)
	v_mfma_f32_32x32x16_f16 v[48:63], v[64:67], v[68:71], v[48:63]
	v_mfma_f32_32x32x16_f16 v[32:47], v[64:67], v[76:79], v[32:47]
	v_mfma_f32_32x32x16_f16 v[16:31], v[64:67], v[82:85], v[16:31]
	s_waitcnt lgkmcnt(4)
	v_mfma_f32_32x32x16_f16 v[0:15], v[64:67], v[90:93], v[0:15]
	global_load_dwordx4 v[64:67], v[110:111], off
	ds_read_b128 v[68:71], v75 offset:192
	ds_read_b128 v[76:79], v75 offset:17088
	ds_read_b128 v[82:85], v75 offset:33984
	ds_read_b128 v[90:93], v75 offset:50880
	s_waitcnt vmcnt(1) lgkmcnt(7)
	v_mfma_f32_32x32x16_f16 v[48:63], v[86:89], v[94:97], v[48:63]
	s_waitcnt lgkmcnt(6)
	v_mfma_f32_32x32x16_f16 v[32:47], v[86:89], v[98:101], v[32:47]
	s_waitcnt lgkmcnt(5)
	v_mfma_f32_32x32x16_f16 v[16:31], v[86:89], v[102:105], v[16:31]
	s_waitcnt lgkmcnt(4)
	v_mfma_f32_32x32x16_f16 v[0:15], v[86:89], v[106:109], v[0:15]
	s_movk_i32 s0, 0x5000
	v_add_co_u32_e32 v110, vcc, s0, v72
	s_nop 1
	v_addc_co_u32_e32 v111, vcc, 0, v73, vcc
	global_load_dwordx4 v[86:89], v[110:111], off offset:-4096
	ds_read_b128 v[94:97], v75 offset:256
	ds_read_b128 v[98:101], v75 offset:17152
	ds_read_b128 v[102:105], v75 offset:34048
	ds_read_b128 v[106:109], v75 offset:50944
	s_waitcnt vmcnt(1) lgkmcnt(7)
	v_mfma_f32_32x32x16_f16 v[48:63], v[64:67], v[68:71], v[48:63]
	s_waitcnt lgkmcnt(6)
	v_mfma_f32_32x32x16_f16 v[32:47], v[64:67], v[76:79], v[32:47]
	s_waitcnt lgkmcnt(5)
	v_mfma_f32_32x32x16_f16 v[16:31], v[64:67], v[82:85], v[16:31]
	s_waitcnt lgkmcnt(4)
	v_mfma_f32_32x32x16_f16 v[0:15], v[64:67], v[90:93], v[0:15]
	global_load_dwordx4 v[64:67], v[110:111], off
	ds_read_b128 v[68:71], v75 offset:320
	ds_read_b128 v[76:79], v75 offset:17216
	ds_read_b128 v[82:85], v75 offset:34112
	ds_read_b128 v[90:93], v75 offset:51008
	s_waitcnt vmcnt(1) lgkmcnt(7)
	v_mfma_f32_32x32x16_f16 v[48:63], v[86:89], v[94:97], v[48:63]
	s_waitcnt lgkmcnt(6)
	v_mfma_f32_32x32x16_f16 v[32:47], v[86:89], v[98:101], v[32:47]
	s_waitcnt lgkmcnt(5)
	v_mfma_f32_32x32x16_f16 v[16:31], v[86:89], v[102:105], v[16:31]
	s_waitcnt lgkmcnt(4)
	v_mfma_f32_32x32x16_f16 v[0:15], v[86:89], v[106:109], v[0:15]
	s_movk_i32 s0, 0x7000
	v_add_co_u32_e32 v72, vcc, s0, v72
	s_nop 1
	v_addc_co_u32_e32 v73, vcc, 0, v73, vcc
	global_load_dwordx4 v[86:89], v[72:73], off offset:-4096
	ds_read_b128 v[94:97], v75 offset:384
	ds_read_b128 v[98:101], v75 offset:17280
	ds_read_b128 v[102:105], v75 offset:34176
	ds_read_b128 v[106:109], v75 offset:51072
	s_waitcnt vmcnt(1) lgkmcnt(7)
	v_mfma_f32_32x32x16_f16 v[48:63], v[64:67], v[68:71], v[48:63]
	s_waitcnt lgkmcnt(6)
	v_mfma_f32_32x32x16_f16 v[32:47], v[64:67], v[76:79], v[32:47]
	s_waitcnt lgkmcnt(5)
	v_mfma_f32_32x32x16_f16 v[16:31], v[64:67], v[82:85], v[16:31]
	s_waitcnt lgkmcnt(4)
	v_mfma_f32_32x32x16_f16 v[0:15], v[64:67], v[90:93], v[0:15]
	global_load_dwordx4 v[64:67], v[72:73], off
	ds_read_b128 v[68:71], v75 offset:448
	ds_read_b128 v[76:79], v75 offset:17344
	ds_read_b128 v[82:85], v75 offset:34240
	ds_read_b128 v[90:93], v75 offset:51136
	s_waitcnt vmcnt(1) lgkmcnt(7)
	v_mfma_f32_32x32x16_f16 v[48:63], v[86:89], v[94:97], v[48:63]
	s_waitcnt lgkmcnt(6)
	v_mfma_f32_32x32x16_f16 v[32:47], v[86:89], v[98:101], v[32:47]
	s_waitcnt lgkmcnt(5)
	v_mfma_f32_32x32x16_f16 v[16:31], v[86:89], v[102:105], v[16:31]
	s_waitcnt lgkmcnt(4)
	v_mfma_f32_32x32x16_f16 v[0:15], v[86:89], v[106:109], v[0:15]
	s_waitcnt vmcnt(0) lgkmcnt(3)
	v_mfma_f32_32x32x16_f16 v[48:63], v[64:67], v[68:71], v[48:63]
	s_waitcnt lgkmcnt(2)
	v_mfma_f32_32x32x16_f16 v[32:47], v[64:67], v[76:79], v[32:47]
	s_waitcnt lgkmcnt(1)
	v_mfma_f32_32x32x16_f16 v[16:31], v[64:67], v[82:85], v[16:31]
	s_waitcnt lgkmcnt(0)
	v_mfma_f32_32x32x16_f16 v[0:15], v[64:67], v[90:93], v[0:15]
	v_readfirstlane_b32 s24, v74
	global_load_dwordx4 v[68:71], v80, s[12:13]
	global_load_dwordx4 v[88:91], v80, s[12:13] offset:32
	global_load_dwordx4 v[92:95], v80, s[12:13] offset:64
	global_load_dwordx4 v[96:99], v80, s[12:13] offset:96
	v_and_b32_e32 v86, 4, v74
	v_lshlrev_b32_e32 v86, 14, v86
	v_lshl_add_u32 v86, v180, 2, v86
	s_lshl_b32 s25, s4, 20
	s_nop 3
	s_lshr_b32 s24, s24, 5
	s_lshl_b32 s24, s24, 19
	s_add_u32 s25, s25, s24
	s_lshl_b32 s24, s20, 8
	s_add_u32 s25, s25, s24
	s_lshl_b32 s24, s5, 2
	s_add_u32 s25, s25, s24
	s_add_u32 s22, s14, s25
	s_addc_u32 s23, s15, 0
	s_waitcnt vmcnt(0)
	v_fmamk_f32 v48, v48, 0x3a800000, v68
	v_fmamk_f32 v32, v32, 0x3a800000, v68
	v_fmamk_f32 v16, v16, 0x3a800000, v68
	v_fmamk_f32 v0, v0, 0x3a800000, v68
	global_store_dword v86, v48, s[22:23]
	global_store_dword v86, v32, s[22:23] offset:256
	global_store_dword v86, v16, s[22:23] offset:512
	global_store_dword v86, v0, s[22:23] offset:768
	s_add_u32 s22, s22, 0x4000
	s_addc_u32 s23, s23, 0
	v_fmamk_f32 v49, v49, 0x3a800000, v69
	v_fmamk_f32 v33, v33, 0x3a800000, v69
	v_fmamk_f32 v17, v17, 0x3a800000, v69
	v_fmamk_f32 v1, v1, 0x3a800000, v69
	global_store_dword v86, v49, s[22:23]
	global_store_dword v86, v33, s[22:23] offset:256
	global_store_dword v86, v17, s[22:23] offset:512
	global_store_dword v86, v1, s[22:23] offset:768
	s_add_u32 s22, s22, 0x4000
	s_addc_u32 s23, s23, 0
	v_fmamk_f32 v50, v50, 0x3a800000, v70
	v_fmamk_f32 v34, v34, 0x3a800000, v70
	v_fmamk_f32 v18, v18, 0x3a800000, v70
	v_fmamk_f32 v2, v2, 0x3a800000, v70
	global_store_dword v86, v50, s[22:23]
	global_store_dword v86, v34, s[22:23] offset:256
	global_store_dword v86, v18, s[22:23] offset:512
	global_store_dword v86, v2, s[22:23] offset:768
	s_add_u32 s22, s22, 0x4000
	s_addc_u32 s23, s23, 0
	v_fmamk_f32 v51, v51, 0x3a800000, v71
	v_fmamk_f32 v35, v35, 0x3a800000, v71
	v_fmamk_f32 v19, v19, 0x3a800000, v71
	v_fmamk_f32 v3, v3, 0x3a800000, v71
	global_store_dword v86, v51, s[22:23]
	global_store_dword v86, v35, s[22:23] offset:256
	global_store_dword v86, v19, s[22:23] offset:512
	global_store_dword v86, v3, s[22:23] offset:768
	s_add_u32 s22, s22, 0x14000
	s_addc_u32 s23, s23, 0
	v_fmamk_f32 v52, v52, 0x3a800000, v88
	v_fmamk_f32 v36, v36, 0x3a800000, v88
	v_fmamk_f32 v20, v20, 0x3a800000, v88
	v_fmamk_f32 v4, v4, 0x3a800000, v88
	global_store_dword v86, v52, s[22:23]
	global_store_dword v86, v36, s[22:23] offset:256
	global_store_dword v86, v20, s[22:23] offset:512
	global_store_dword v86, v4, s[22:23] offset:768
	s_add_u32 s22, s22, 0x4000
	s_addc_u32 s23, s23, 0
	v_fmamk_f32 v53, v53, 0x3a800000, v89
	v_fmamk_f32 v37, v37, 0x3a800000, v89
	v_fmamk_f32 v21, v21, 0x3a800000, v89
	v_fmamk_f32 v5, v5, 0x3a800000, v89
	global_store_dword v86, v53, s[22:23]
	global_store_dword v86, v37, s[22:23] offset:256
	global_store_dword v86, v21, s[22:23] offset:512
	global_store_dword v86, v5, s[22:23] offset:768
	s_add_u32 s22, s22, 0x4000
	s_addc_u32 s23, s23, 0
	v_fmamk_f32 v54, v54, 0x3a800000, v90
	v_fmamk_f32 v38, v38, 0x3a800000, v90
	v_fmamk_f32 v22, v22, 0x3a800000, v90
	v_fmamk_f32 v6, v6, 0x3a800000, v90
	global_store_dword v86, v54, s[22:23]
	global_store_dword v86, v38, s[22:23] offset:256
	global_store_dword v86, v22, s[22:23] offset:512
	global_store_dword v86, v6, s[22:23] offset:768
	s_add_u32 s22, s22, 0x4000
	s_addc_u32 s23, s23, 0
	v_fmamk_f32 v55, v55, 0x3a800000, v91
	v_fmamk_f32 v39, v39, 0x3a800000, v91
	v_fmamk_f32 v23, v23, 0x3a800000, v91
	v_fmamk_f32 v7, v7, 0x3a800000, v91
	global_store_dword v86, v55, s[22:23]
	global_store_dword v86, v39, s[22:23] offset:256
	global_store_dword v86, v23, s[22:23] offset:512
	global_store_dword v86, v7, s[22:23] offset:768
	s_add_u32 s22, s22, 0x14000
	s_addc_u32 s23, s23, 0
	v_fmamk_f32 v56, v56, 0x3a800000, v92
	v_fmamk_f32 v40, v40, 0x3a800000, v92
	v_fmamk_f32 v24, v24, 0x3a800000, v92
	v_fmamk_f32 v8, v8, 0x3a800000, v92
	global_store_dword v86, v56, s[22:23]
	global_store_dword v86, v40, s[22:23] offset:256
	global_store_dword v86, v24, s[22:23] offset:512
	global_store_dword v86, v8, s[22:23] offset:768
	s_add_u32 s22, s22, 0x4000
	s_addc_u32 s23, s23, 0
	v_fmamk_f32 v57, v57, 0x3a800000, v93
	v_fmamk_f32 v41, v41, 0x3a800000, v93
	v_fmamk_f32 v25, v25, 0x3a800000, v93
	v_fmamk_f32 v9, v9, 0x3a800000, v93
	global_store_dword v86, v57, s[22:23]
	global_store_dword v86, v41, s[22:23] offset:256
	global_store_dword v86, v25, s[22:23] offset:512
	global_store_dword v86, v9, s[22:23] offset:768
	s_add_u32 s22, s22, 0x4000
	s_addc_u32 s23, s23, 0
	v_fmamk_f32 v58, v58, 0x3a800000, v94
	v_fmamk_f32 v42, v42, 0x3a800000, v94
	v_fmamk_f32 v26, v26, 0x3a800000, v94
	v_fmamk_f32 v10, v10, 0x3a800000, v94
	global_store_dword v86, v58, s[22:23]
	global_store_dword v86, v42, s[22:23] offset:256
	global_store_dword v86, v26, s[22:23] offset:512
	global_store_dword v86, v10, s[22:23] offset:768
	s_add_u32 s22, s22, 0x4000
	s_addc_u32 s23, s23, 0
	v_fmamk_f32 v59, v59, 0x3a800000, v95
	v_fmamk_f32 v43, v43, 0x3a800000, v95
	v_fmamk_f32 v27, v27, 0x3a800000, v95
	v_fmamk_f32 v11, v11, 0x3a800000, v95
	global_store_dword v86, v59, s[22:23]
	global_store_dword v86, v43, s[22:23] offset:256
	global_store_dword v86, v27, s[22:23] offset:512
	global_store_dword v86, v11, s[22:23] offset:768
	s_add_u32 s22, s22, 0x14000
	s_addc_u32 s23, s23, 0
	v_fmamk_f32 v60, v60, 0x3a800000, v96
	v_fmamk_f32 v44, v44, 0x3a800000, v96
	v_fmamk_f32 v28, v28, 0x3a800000, v96
	v_fmamk_f32 v12, v12, 0x3a800000, v96
	global_store_dword v86, v60, s[22:23]
	global_store_dword v86, v44, s[22:23] offset:256
	global_store_dword v86, v28, s[22:23] offset:512
	global_store_dword v86, v12, s[22:23] offset:768
	s_add_u32 s22, s22, 0x4000
	s_addc_u32 s23, s23, 0
	v_fmamk_f32 v61, v61, 0x3a800000, v97
	v_fmamk_f32 v45, v45, 0x3a800000, v97
	v_fmamk_f32 v29, v29, 0x3a800000, v97
	v_fmamk_f32 v13, v13, 0x3a800000, v97
	global_store_dword v86, v61, s[22:23]
	global_store_dword v86, v45, s[22:23] offset:256
	global_store_dword v86, v29, s[22:23] offset:512
	global_store_dword v86, v13, s[22:23] offset:768
	s_add_u32 s22, s22, 0x4000
	s_addc_u32 s23, s23, 0
	v_fmamk_f32 v62, v62, 0x3a800000, v98
	v_fmamk_f32 v46, v46, 0x3a800000, v98
	v_fmamk_f32 v30, v30, 0x3a800000, v98
	v_fmamk_f32 v14, v14, 0x3a800000, v98
	global_store_dword v86, v62, s[22:23]
	global_store_dword v86, v46, s[22:23] offset:256
	global_store_dword v86, v30, s[22:23] offset:512
	global_store_dword v86, v14, s[22:23] offset:768
	s_add_u32 s22, s22, 0x4000
	s_addc_u32 s23, s23, 0
	v_fmamk_f32 v63, v63, 0x3a800000, v99
	v_fmamk_f32 v47, v47, 0x3a800000, v99
	v_fmamk_f32 v31, v31, 0x3a800000, v99
	v_fmamk_f32 v15, v15, 0x3a800000, v99
	global_store_dword v86, v63, s[22:23]
	global_store_dword v86, v47, s[22:23] offset:256
	global_store_dword v86, v31, s[22:23] offset:512
	global_store_dword v86, v15, s[22:23] offset:768
